# G1: next-unit tile decode (division chain, next A/B pointers) computed inside the peeled first K-iteration between MFMAs instead of serially at each unit top
# speedup vs baseline: 1.0055x; 1.0007x over previous
; #define PG8_STAGE(bufoff, gbase, voff) do { _Pragma("unroll") for (int _i = 0; _i < 2; ++_i) \
;         __builtin_amdgcn_global_load_lds((const unsigned*)((const char*)(gbase) + (voff)[_i]), (PG8_LAS unsigned*)(lds + (bufoff) + ldsw + _i * 8192), 16, 0, 0); } while (0)
; #define PG8_LDA(dst, b, h) do { _Pragma("unroll") for (int m = 0; m < 4; ++m) _Pragma("unroll") for (int k = 0; k < 2; ++k) dst[m][k] = *(const PG8_LAS bf16x8*)(lds + PG8_SA(b, h) + aoff + m * 2048 + k * 1024); } while (0)
;     __host__ __device__ bool next(int i, Unit& u) const {
;         const long L = (long)i * G + c; if (L >= nwg) return false;
;         int wgid = (int)L; { const int q = nwg / NXCD, r = nwg % NXCD, xcd = wgid % NXCD, off = wgid / NXCD; wgid = (xcd < r ? xcd * (q + 1) : r * (q + 1) + (xcd - r) * q) + off; }
;         const int nig = WGM * nN, gid = wgid / nig, fm = gid * WGM, gsz = (nM - fm) < WGM ? (nM - fm) : WGM;
;         u.pm = fm + ((wgid % nig) % gsz); u.pn = (wgid % nig) / gsz; u.idx = i; return true;
; template <class Epi, class Sched, bool ALIGN_EPI = false, bool SP2 = false>
; __device__ __forceinline__ void gemm_phase(PG8_LAS unsigned char* lds, const Gemm g, const Sched& S, const Epi& E, const int tid) {
;     ...
;         const bool has_next = S.next(ui + 1, nxt);
;         const char* nA = has_next ? (const char*)g.A + (size_t)nxt.pm * tstep : cA; const char* nB = has_next ? (const char*)g.Bt + (size_t)nxt.pn * tstep : cB;
;         for (int t = 0; t < nt; t += 2) {
;             const bool last = (t == nt - 2);
;             const char* a1 = cA + (size_t)(t + 1) * kstep;
;             const char* a2 = last ? nA : cA + (size_t)(t + 2) * kstep; const char* b2 = last ? nB : cB + (size_t)(t + 2) * kstep;
;             const char* a3 = a2 + kstep; const char* b3 = b2 + kstep;
;             if (last && has_next) S.a_ready(nxt);
;             if constexpr (SP2) {
;             PG8_LDB(B0, 0, 0); PG8_LDB(B1, 0, 1); PG8_SCHED; PG8_LDA(At, 0, 0); PG8_STAGE(PG8_SA(1, 1), a1 + hstep, voffA);
;             PG8_WAIT_V(8); PG8_WAIT_L(0); PG8_BAR; PG8_MMA(0, 0, At, B0); PG8_MMA(0, 1, At, B1); PG8_BAR; PG8_SCHED;
;             PG8_LDA(At, 0, 1); PG8_STAGE(PG8_SB(0, 0), b2, voffB); PG8_STAGE(PG8_SB(0, 1), b2, voffB1); PG8_STAGE(PG8_SA(0, 0), a2, voffA);
;             PG8_WAIT_V(8); PG8_WAIT_L(0); PG8_BAR; PG8_MMA(1, 0, At, B0); PG8_MMA(1, 1, At, B1); PG8_BAR; PG8_SCHED;
.LBB0_724:
.LBB0_726:
	s_add_u32 s46, s46, 0x40080
	s_addc_u32 s47, s47, 0
	s_add_u32 s52, s52, 0x100
	s_addc_u32 s53, s53, 0
	s_mov_b32 s62, -2
	s_add_u32 s36, s46, 0xfffc0080
	s_addc_u32 s37, s47, -1
	s_add_i32 s63, 0, 0x10000
	s_cmp_eq_u32 s62, 12
	s_cselect_b32 s37, s11, s37
	s_cselect_b32 s36, s59, s36
	v_add_u32_e32 v148, s63, v151
	s_cselect_b32 s73, s9, s53
	s_cselect_b32 s72, s60, s52
	s_add_i32 s68, 0, 0x14000
	ds_read_b128 v[144:147], v148
	ds_read_b128 v[156:159], v148 offset:1024
	ds_read_b128 v[160:163], v148 offset:2048
	ds_read_b128 v[164:167], v148 offset:3072
	v_add_u32_e32 v148, s68, v151
	ds_read_b128 v[168:171], v148
	ds_read_b128 v[172:175], v148 offset:1024
	ds_read_b128 v[176:179], v148 offset:2048
	ds_read_b128 v[180:183], v148 offset:3072
	v_lshl_add_u64 v[148:149], s[46:47], 0, v[140:141]
	s_add_i32 m0, s43, 0xc000
	ds_read_b128 v[184:187], v154
	ds_read_b128 v[188:191], v154 offset:1024
	ds_read_b128 v[192:195], v154 offset:2048
	ds_read_b128 v[196:199], v154 offset:3072
	ds_read_b128 v[212:215], v154 offset:4096
	ds_read_b128 v[216:219], v154 offset:5120
	ds_read_b128 v[220:223], v154 offset:6144
	ds_read_b128 v[224:227], v154 offset:7168
	global_load_lds_dwordx4 v[148:149], off
	v_lshl_add_u64 v[148:149], s[46:47], 0, v[142:143]
	s_add_i32 m0, s43, 0xe000
	s_nop 0
	global_load_lds_dwordx4 v[148:149], off
	s_waitcnt vmcnt(8)
	s_waitcnt lgkmcnt(0)
	s_barrier
	s_setprio 1
	s_waitcnt lgkmcnt(0)
	v_mfma_f32_16x16x32_bf16 v[128:131], v[144:147], v[184:187], 0
	v_mfma_f32_16x16x32_bf16 v[120:123], v[160:163], v[184:187], 0
	v_mfma_f32_16x16x32_bf16 v[112:115], v[144:147], v[192:195], 0
	v_mfma_f32_16x16x32_bf16 v[104:107], v[160:163], v[192:195], 0
	v_mfma_f32_16x16x32_bf16 v[96:99], v[144:147], v[212:215], 0
	v_mfma_f32_16x16x32_bf16 v[88:91], v[160:163], v[212:215], 0
	v_mfma_f32_16x16x32_bf16 v[80:83], v[144:147], v[220:223], 0
	v_mfma_f32_16x16x32_bf16 v[72:75], v[160:163], v[220:223], 0
	v_mfma_f32_16x16x32_bf16 v[128:131], v[156:159], v[188:191], v[128:131]
	v_mfma_f32_16x16x32_bf16 v[120:123], v[164:167], v[188:191], v[120:123]
	v_mfma_f32_16x16x32_bf16 v[112:115], v[156:159], v[196:199], v[112:115]
	v_mfma_f32_16x16x32_bf16 v[104:107], v[164:167], v[196:199], v[104:107]
	v_mfma_f32_16x16x32_bf16 v[96:99], v[156:159], v[216:219], v[96:99]
	v_mfma_f32_16x16x32_bf16 v[88:91], v[164:167], v[216:219], v[88:91]
	v_mfma_f32_16x16x32_bf16 v[80:83], v[156:159], v[224:227], v[80:83]
	v_mfma_f32_16x16x32_bf16 v[72:75], v[164:167], v[224:227], v[72:75]
	s_setprio 0
	s_setprio 1
	v_mfma_f32_16x16x32_bf16 v[124:127], v[168:171], v[184:187], 0
	v_mfma_f32_16x16x32_bf16 v[116:119], v[176:179], v[184:187], 0
	v_mfma_f32_16x16x32_bf16 v[108:111], v[168:171], v[192:195], 0
	v_mfma_f32_16x16x32_bf16 v[100:103], v[176:179], v[192:195], 0
	v_mfma_f32_16x16x32_bf16 v[92:95], v[168:171], v[212:215], 0
	v_mfma_f32_16x16x32_bf16 v[84:87], v[176:179], v[212:215], 0
	v_mfma_f32_16x16x32_bf16 v[76:79], v[168:171], v[220:223], 0
	v_mfma_f32_16x16x32_bf16 v[68:71], v[176:179], v[220:223], 0
	v_mfma_f32_16x16x32_bf16 v[124:127], v[172:175], v[188:191], v[124:127]
	v_mfma_f32_16x16x32_bf16 v[116:119], v[180:183], v[188:191], v[116:119]
	v_mfma_f32_16x16x32_bf16 v[108:111], v[172:175], v[196:199], v[108:111]
	v_mfma_f32_16x16x32_bf16 v[100:103], v[180:183], v[196:199], v[100:103]
	v_mfma_f32_16x16x32_bf16 v[92:95], v[172:175], v[216:219], v[92:95]
	v_mfma_f32_16x16x32_bf16 v[84:87], v[180:183], v[216:219], v[84:87]
	v_mfma_f32_16x16x32_bf16 v[76:79], v[172:175], v[224:227], v[76:79]
	v_mfma_f32_16x16x32_bf16 v[68:71], v[180:183], v[224:227], v[68:71]
	s_setprio 0
	s_barrier
	s_add_i32 s63, s63, s33
	v_lshl_add_u64 v[148:149], s[72:73], 0, v[2:3]
	s_mov_b32 m0, s63
	ds_read_b128 v[184:187], v154 offset:16384
	ds_read_b128 v[188:191], v154 offset:17408
	ds_read_b128 v[192:195], v154 offset:18432
	ds_read_b128 v[196:199], v154 offset:19456
	ds_read_b128 v[212:215], v154 offset:20480
	ds_read_b128 v[216:219], v154 offset:21504
	ds_read_b128 v[220:223], v154 offset:22528
	ds_read_b128 v[224:227], v154 offset:23552
	global_load_lds_dwordx4 v[148:149], off
	v_lshl_add_u64 v[200:201], s[72:73], 0, v[132:133]
	s_add_i32 m0, s63, 0x2000
	s_add_i32 s63, s68, s33
	global_load_lds_dwordx4 v[200:201], off
	v_lshl_add_u64 v[202:203], s[72:73], 0, v[136:137]
	s_mov_b32 m0, s63
	v_lshl_add_u64 v[204:205], s[72:73], 0, v[0:1]
	global_load_lds_dwordx4 v[202:203], off
	s_add_i32 m0, s63, 0x2000
	v_lshl_add_u64 v[208:209], s[36:37], 0, v[138:139]
	global_load_lds_dwordx4 v[204:205], off
	s_mov_b32 m0, s43
	v_lshl_add_u64 v[210:211], s[36:37], 0, v[134:135]
	global_load_lds_dwordx4 v[208:209], off
	s_mov_b32 m0, s45
	s_nop 0
	global_load_lds_dwordx4 v[210:211], off
	s_waitcnt vmcnt(8)
	s_waitcnt lgkmcnt(0)
	s_barrier
; #define PG8_STAGE(bufoff, gbase, voff) do { _Pragma("unroll") for (int _i = 0; _i < 2; ++_i) \
;         __builtin_amdgcn_global_load_lds((const unsigned*)((const char*)(gbase) + (voff)[_i]), (PG8_LAS unsigned*)(lds + (bufoff) + ldsw + _i * 8192), 16, 0, 0); } while (0)
; #define PG8_LDA(dst, b, h) do { _Pragma("unroll") for (int m = 0; m < 4; ++m) _Pragma("unroll") for (int k = 0; k < 2; ++k) dst[m][k] = *(const PG8_LAS bf16x8*)(lds + PG8_SA(b, h) + aoff + m * 2048 + k * 1024); } while (0)
; #define PG8_LDB(dst, b, h) do { _Pragma("unroll") for (int n = 0; n < 2; ++n) _Pragma("unroll") for (int k = 0; k < 2; ++k) dst[n][k] = *(const PG8_LAS bf16x8*)(lds + PG8_SB(b, h) + boff + n * 2048 + k * 1024); } while (0)
; #define PG8_MMA(ai, bj, At, Bt) do { __builtin_amdgcn_s_setprio(1); _Pragma("unroll") for (int m = 0; m < 4; ++m) _Pragma("unroll") for (int n = 0; n < 2; ++n) _Pragma("unroll") for (int k = 0; k < 2; ++k) \
;         acc[ai][bj][m][n] = __builtin_amdgcn_mfma_f32_16x16x32_bf16(Bt[n][k], At[m][k], acc[ai][bj][m][n], 0, 0, 0); __builtin_amdgcn_s_setprio(0); } while (0)
; #define PG8_WAIT_V(n) asm volatile("s_waitcnt vmcnt(" #n ")" ::: "memory")
; #define PG8_WAIT_L(n) asm volatile("s_waitcnt lgkmcnt(" #n ")" ::: "memory")
; #define PG8_BAR __builtin_amdgcn_s_barrier()
; #define PG8_SCHED __builtin_amdgcn_sched_barrier(0)
; template <class Epi, class Sched, bool ALIGN_EPI = false, bool SP2 = false>
; __device__ __forceinline__ void gemm_phase(PG8_LAS unsigned char* lds, const Gemm g, const Sched& S, const Epi& E, const int tid) {
;     ...
;             PG8_WAIT_V(8); PG8_WAIT_L(0); PG8_BAR; PG8_MMA(1, 0, At, B0); PG8_MMA(1, 1, At, B1); PG8_BAR; PG8_SCHED;
;             PG8_LDB(B0, 1, 0); PG8_LDB(B1, 1, 1); PG8_SCHED; PG8_LDA(At, 1, 0); PG8_STAGE(PG8_SA(0, 1), a2 + hstep, voffA);
;             PG8_WAIT_V(8); PG8_WAIT_L(0); PG8_BAR; PG8_MMA(0, 0, At, B0); PG8_MMA(0, 1, At, B1); PG8_BAR; PG8_SCHED;
	s_setprio 1
	s_waitcnt lgkmcnt(0)
	v_mfma_f32_16x16x32_bf16 v[64:67], v[144:147], v[184:187], 0
	v_mfma_f32_16x16x32_bf16 v[56:59], v[160:163], v[184:187], 0
	v_mfma_f32_16x16x32_bf16 v[48:51], v[144:147], v[192:195], 0
	v_mfma_f32_16x16x32_bf16 v[40:43], v[160:163], v[192:195], 0
	v_mfma_f32_16x16x32_bf16 v[32:35], v[144:147], v[212:215], 0
	v_mfma_f32_16x16x32_bf16 v[24:27], v[160:163], v[212:215], 0
	v_mfma_f32_16x16x32_bf16 v[16:19], v[144:147], v[220:223], 0
	v_mfma_f32_16x16x32_bf16 v[8:11], v[160:163], v[220:223], 0
	v_mfma_f32_16x16x32_bf16 v[64:67], v[156:159], v[188:191], v[64:67]
	v_mfma_f32_16x16x32_bf16 v[56:59], v[164:167], v[188:191], v[56:59]
	v_mfma_f32_16x16x32_bf16 v[48:51], v[156:159], v[196:199], v[48:51]
	v_mfma_f32_16x16x32_bf16 v[40:43], v[164:167], v[196:199], v[40:43]
	v_mfma_f32_16x16x32_bf16 v[32:35], v[156:159], v[216:219], v[32:35]
	v_mfma_f32_16x16x32_bf16 v[24:27], v[164:167], v[216:219], v[24:27]
	v_mfma_f32_16x16x32_bf16 v[16:19], v[156:159], v[224:227], v[16:19]
	v_mfma_f32_16x16x32_bf16 v[8:11], v[164:167], v[224:227], v[8:11]
	s_setprio 0
	s_setprio 1
	v_mfma_f32_16x16x32_bf16 v[60:63], v[168:171], v[184:187], 0
	v_mfma_f32_16x16x32_bf16 v[52:55], v[176:179], v[184:187], 0
	v_mfma_f32_16x16x32_bf16 v[44:47], v[168:171], v[192:195], 0
	v_mfma_f32_16x16x32_bf16 v[36:39], v[176:179], v[192:195], 0
	v_mfma_f32_16x16x32_bf16 v[28:31], v[168:171], v[212:215], 0
	v_mfma_f32_16x16x32_bf16 v[20:23], v[176:179], v[212:215], 0
	v_mfma_f32_16x16x32_bf16 v[12:15], v[168:171], v[220:223], 0
	v_mfma_f32_16x16x32_bf16 v[4:7], v[176:179], v[220:223], 0
	v_mfma_f32_16x16x32_bf16 v[60:63], v[172:175], v[188:191], v[60:63]
	v_mfma_f32_16x16x32_bf16 v[52:55], v[180:183], v[188:191], v[52:55]
	v_mfma_f32_16x16x32_bf16 v[44:47], v[172:175], v[196:199], v[44:47]
	v_mfma_f32_16x16x32_bf16 v[36:39], v[180:183], v[196:199], v[36:39]
	v_mfma_f32_16x16x32_bf16 v[28:31], v[172:175], v[216:219], v[28:31]
	v_mfma_f32_16x16x32_bf16 v[20:23], v[180:183], v[216:219], v[20:23]
	v_mfma_f32_16x16x32_bf16 v[12:15], v[172:175], v[224:227], v[12:15]
	v_mfma_f32_16x16x32_bf16 v[4:7], v[180:183], v[224:227], v[4:7]
	s_setprio 0
	s_barrier
	s_add_i32 s63, 0, 0x18000
	v_add_u32_e32 v155, s63, v151
	s_add_i32 s68, 0, 0x1c000
	ds_read_b128 v[144:147], v155
	ds_read_b128 v[156:159], v155 offset:1024
	ds_read_b128 v[160:163], v155 offset:2048
	ds_read_b128 v[164:167], v155 offset:3072
	v_add_u32_e32 v155, s68, v151
	ds_read_b128 v[168:171], v155
	ds_read_b128 v[172:175], v155 offset:1024
	ds_read_b128 v[176:179], v155 offset:2048
	ds_read_b128 v[180:183], v155 offset:3072
	s_add_u32 s36, s36, 0x40000
	s_addc_u32 s37, s37, 0
	s_mov_b32 m0, s48
	v_lshl_add_u64 v[228:229], s[36:37], 0, v[138:139]
	ds_read_b128 v[184:187], v154 offset:32768
	ds_read_b128 v[188:191], v154 offset:33792
	ds_read_b128 v[192:195], v154 offset:34816
	ds_read_b128 v[196:199], v154 offset:35840
	ds_read_b128 v[212:215], v154 offset:36864
	ds_read_b128 v[216:219], v154 offset:37888
	ds_read_b128 v[220:223], v154 offset:38912
	ds_read_b128 v[224:227], v154 offset:39936
	global_load_lds_dwordx4 v[228:229], off
	v_lshl_add_u64 v[228:229], s[36:37], 0, v[134:135]
	s_mov_b32 m0, s49
	s_nop 0
	global_load_lds_dwordx4 v[228:229], off
	s_waitcnt vmcnt(8)
	s_waitcnt lgkmcnt(0)
	s_barrier
	s_setprio 1
	s_waitcnt lgkmcnt(0)
	v_mfma_f32_16x16x32_bf16 v[128:131], v[144:147], v[184:187], v[128:131]
	v_mfma_f32_16x16x32_bf16 v[120:123], v[160:163], v[184:187], v[120:123]
	v_mfma_f32_16x16x32_bf16 v[112:115], v[144:147], v[192:195], v[112:115]
	v_mfma_f32_16x16x32_bf16 v[104:107], v[160:163], v[192:195], v[104:107]
	v_mfma_f32_16x16x32_bf16 v[96:99], v[144:147], v[212:215], v[96:99]
	v_mfma_f32_16x16x32_bf16 v[88:91], v[160:163], v[212:215], v[88:91]
	v_mfma_f32_16x16x32_bf16 v[80:83], v[144:147], v[220:223], v[80:83]
	v_mfma_f32_16x16x32_bf16 v[72:75], v[160:163], v[220:223], v[72:75]
	v_mfma_f32_16x16x32_bf16 v[128:131], v[156:159], v[188:191], v[128:131]
	v_mfma_f32_16x16x32_bf16 v[120:123], v[164:167], v[188:191], v[120:123]
	v_mfma_f32_16x16x32_bf16 v[112:115], v[156:159], v[196:199], v[112:115]
	v_mfma_f32_16x16x32_bf16 v[104:107], v[164:167], v[196:199], v[104:107]
	v_mfma_f32_16x16x32_bf16 v[96:99], v[156:159], v[216:219], v[96:99]
	v_mfma_f32_16x16x32_bf16 v[88:91], v[164:167], v[216:219], v[88:91]
	v_mfma_f32_16x16x32_bf16 v[80:83], v[156:159], v[224:227], v[80:83]
	v_mfma_f32_16x16x32_bf16 v[72:75], v[164:167], v[224:227], v[72:75]
	s_setprio 0
	s_setprio 1
	v_mfma_f32_16x16x32_bf16 v[124:127], v[168:171], v[184:187], v[124:127]
	v_mfma_f32_16x16x32_bf16 v[116:119], v[176:179], v[184:187], v[116:119]
	v_mfma_f32_16x16x32_bf16 v[108:111], v[168:171], v[192:195], v[108:111]
	v_mfma_f32_16x16x32_bf16 v[100:103], v[176:179], v[192:195], v[100:103]
	v_mfma_f32_16x16x32_bf16 v[92:95], v[168:171], v[212:215], v[92:95]
	v_mfma_f32_16x16x32_bf16 v[84:87], v[176:179], v[212:215], v[84:87]
	v_mfma_f32_16x16x32_bf16 v[76:79], v[168:171], v[220:223], v[76:79]
	v_mfma_f32_16x16x32_bf16 v[68:71], v[176:179], v[220:223], v[68:71]
	v_mfma_f32_16x16x32_bf16 v[124:127], v[172:175], v[188:191], v[124:127]
	v_mfma_f32_16x16x32_bf16 v[116:119], v[180:183], v[188:191], v[116:119]
	v_mfma_f32_16x16x32_bf16 v[108:111], v[172:175], v[196:199], v[108:111]
	v_mfma_f32_16x16x32_bf16 v[100:103], v[180:183], v[196:199], v[100:103]
	v_mfma_f32_16x16x32_bf16 v[92:95], v[172:175], v[216:219], v[92:95]
	v_mfma_f32_16x16x32_bf16 v[84:87], v[180:183], v[216:219], v[84:87]
	v_mfma_f32_16x16x32_bf16 v[76:79], v[172:175], v[224:227], v[76:79]
	v_mfma_f32_16x16x32_bf16 v[68:71], v[180:183], v[224:227], v[68:71]
	s_setprio 0
	s_barrier
; #define PG8_BAR __builtin_amdgcn_s_barrier()
;     __host__ __device__ bool next(int i, Unit& u) const {
;         const long L = (long)i * G + c; if (L >= nwg) return false;
;         int wgid = (int)L; { const int q = nwg / NXCD, r = nwg % NXCD, xcd = wgid % NXCD, off = wgid / NXCD; wgid = (xcd < r ? xcd * (q + 1) : r * (q + 1) + (xcd - r) * q) + off; }
;         const int nig = WGM * nN, gid = wgid / nig, fm = gid * WGM, gsz = (nM - fm) < WGM ? (nM - fm) : WGM;
;         u.pm = fm + ((wgid % nig) % gsz); u.pn = (wgid % nig) / gsz; u.idx = i; return true;
; template <class Epi, class Sched, bool ALIGN_EPI = false, bool SP2 = false>
; __device__ __forceinline__ void gemm_phase(PG8_LAS unsigned char* lds, const Gemm g, const Sched& S, const Epi& E, const int tid) {
;     ...
;         const char* nA = has_next ? (const char*)g.A + (size_t)nxt.pm * tstep : cA; const char* nB = has_next ? (const char*)g.Bt + (size_t)nxt.pn * tstep : cB;
;         for (int t = 0; t < nt; t += 2) {
;             const bool last = (t == nt - 2);
;             const char* a1 = cA + (size_t)(t + 1) * kstep;
;             const char* a2 = last ? nA : cA + (size_t)(t + 2) * kstep; const char* b2 = last ? nB : cB + (size_t)(t + 2) * kstep;
;             const char* a3 = a2 + kstep; const char* b3 = b2 + kstep;
;             if (last && has_next) S.a_ready(nxt);
;             if constexpr (SP2) {
;             PG8_LDB(B0, 0, 0); PG8_LDB(B1, 0, 1); PG8_SCHED; PG8_LDA(At, 0, 0); PG8_STAGE(PG8_SA(1, 1), a1 + hstep, voffA);
;             PG8_WAIT_V(8); PG8_WAIT_L(0); PG8_BAR; PG8_MMA(0, 0, At, B0); PG8_MMA(0, 1, At, B1); PG8_BAR; PG8_SCHED;
;             PG8_LDA(At, 0, 1); PG8_STAGE(PG8_SB(0, 0), b2, voffB); PG8_STAGE(PG8_SB(0, 1), b2, voffB1); PG8_STAGE(PG8_SA(0, 0), a2, voffA);
;             PG8_WAIT_V(8); PG8_WAIT_L(0); PG8_BAR; PG8_MMA(1, 0, At, B0); PG8_MMA(1, 1, At, B1); PG8_BAR; PG8_SCHED;
;             PG8_LDB(B0, 1, 0); PG8_LDB(B1, 1, 1); PG8_SCHED; PG8_LDA(At, 1, 0); PG8_STAGE(PG8_SA(0, 1), a2 + hstep, voffA);
;             PG8_WAIT_V(8); PG8_WAIT_L(0); PG8_BAR; PG8_MMA(0, 0, At, B0); PG8_MMA(0, 1, At, B1); PG8_BAR; PG8_SCHED;
;             PG8_LDA(At, 1, 1); PG8_STAGE(PG8_SB(1, 0), b3, voffB); PG8_STAGE(PG8_SB(1, 1), b3, voffB1); PG8_STAGE(PG8_SA(1, 0), a3, voffA);
;             PG8_WAIT_V(8); PG8_WAIT_L(0); PG8_BAR; PG8_MMA(1, 0, At, B0); PG8_MMA(1, 1, At, B1); PG8_BAR; PG8_SCHED;
	s_add_i32 s36, s63, s33
	v_lshl_add_u64 v[148:149], v[148:149], 0, s[66:67]
	s_mov_b32 m0, s36
	ds_read_b128 v[184:187], v154 offset:49152
	ds_read_b128 v[188:191], v154 offset:50176
	ds_read_b128 v[192:195], v154 offset:51200
	ds_read_b128 v[196:199], v154 offset:52224
	ds_read_b128 v[212:215], v154 offset:53248
	ds_read_b128 v[216:219], v154 offset:54272
	ds_read_b128 v[220:223], v154 offset:55296
	ds_read_b128 v[224:227], v154 offset:56320
	global_load_lds_dwordx4 v[148:149], off
	v_lshl_add_u64 v[148:149], v[200:201], 0, s[66:67]
	s_add_i32 m0, s36, 0x2000
	s_add_i32 s36, s68, s33
	global_load_lds_dwordx4 v[148:149], off
	v_lshl_add_u64 v[148:149], v[202:203], 0, s[66:67]
	s_mov_b32 m0, s36
	s_nop 0
	global_load_lds_dwordx4 v[148:149], off
	v_lshl_add_u64 v[148:149], v[204:205], 0, s[66:67]
	s_add_i32 m0, s36, 0x2000
	s_nop 0
	global_load_lds_dwordx4 v[148:149], off
	v_lshl_add_u64 v[148:149], v[208:209], 0, s[66:67]
	s_mov_b32 m0, s50
	s_nop 0
	global_load_lds_dwordx4 v[148:149], off
	v_lshl_add_u64 v[148:149], v[210:211], 0, s[66:67]
	s_mov_b32 m0, s51
	s_nop 0
	global_load_lds_dwordx4 v[148:149], off
	s_waitcnt vmcnt(8)
	s_waitcnt lgkmcnt(0)
	s_barrier
	s_setprio 1
	s_waitcnt lgkmcnt(0)
	v_mfma_f32_16x16x32_bf16 v[64:67], v[144:147], v[184:187], v[64:67]
	s_add_i32 s55, s55, 1
	s_mul_i32 s2, s55, s54
	s_mul_hi_u32 s3, s55, s88
	v_mfma_f32_16x16x32_bf16 v[56:59], v[160:163], v[184:187], v[56:59]
	s_add_i32 s3, s3, s2
	s_mul_i32 s2, s55, s88
	s_add_u32 s12, s2, s90
	v_mfma_f32_16x16x32_bf16 v[48:51], v[144:147], v[192:195], v[48:51]
	s_addc_u32 s13, s3, s42
	v_mov_b64_e32 v[242:243], 0xb00
	v_cmp_lt_i64_e64 s[2:3], s[12:13], v[242:243]
	v_mfma_f32_16x16x32_bf16 v[40:43], v[160:163], v[192:195], v[40:43]
	s_ashr_i32 s8, s12, 31
	s_lshr_b32 s8, s8, 29
	s_add_i32 s8, s12, s8
	v_mfma_f32_16x16x32_bf16 v[32:35], v[144:147], v[212:215], v[32:35]
	s_ashr_i32 s9, s8, 3
	s_and_b32 s8, s8, -8
	s_sub_i32 s8, s12, s8
	v_mfma_f32_16x16x32_bf16 v[24:27], v[160:163], v[212:215], v[24:27]
	s_cmp_lt_i32 s8, 0
	s_movk_i32 s10, 0x161
	s_cselect_b32 s10, s10, 0x160
	v_mfma_f32_16x16x32_bf16 v[16:19], v[144:147], v[220:223], v[16:19]
	s_mul_i32 s8, s8, s10
	s_add_i32 s8, s8, s9
	s_mul_hi_i32 s9, s8, 0x2e8ba2e9
	v_mfma_f32_16x16x32_bf16 v[8:11], v[160:163], v[220:223], v[8:11]
	s_lshr_b32 s10, s9, 31
	s_ashr_i32 s9, s9, 5
	s_add_i32 s9, s9, s10
	v_mfma_f32_16x16x32_bf16 v[64:67], v[156:159], v[188:191], v[64:67]
	s_lshl_b32 s10, s9, 3
	s_sub_i32 s11, 0x80, s10
	s_min_i32 s11, s11, 8
	v_mfma_f32_16x16x32_bf16 v[56:59], v[164:167], v[188:191], v[56:59]
	s_abs_i32 s12, s11
	v_cvt_f32_u32_e32 v241, s12
	s_sub_i32 s14, 0, s12
	v_mfma_f32_16x16x32_bf16 v[48:51], v[156:159], v[196:199], v[48:51]
	s_mulk_i32 s9, 0xb0
	s_sub_i32 s9, s8, s9
	v_rcp_iflag_f32_e32 v241, v241
	v_mfma_f32_16x16x32_bf16 v[40:43], v[164:167], v[196:199], v[40:43]
	s_abs_i32 s8, s9
	s_xor_b32 s13, s9, s11
	v_mfma_f32_16x16x32_bf16 v[32:35], v[156:159], v[216:219], v[32:35]
	s_ashr_i32 s13, s13, 31
	v_mul_f32_e32 v241, 0x4f7ffffe, v241
	v_mfma_f32_16x16x32_bf16 v[24:27], v[164:167], v[216:219], v[24:27]
	v_cvt_u32_f32_e32 v241, v241
	s_mov_b32 s56, s55
	v_mfma_f32_16x16x32_bf16 v[16:19], v[156:159], v[224:227], v[16:19]
	v_readfirstlane_b32 s15, v241
	s_mul_i32 s14, s14, s15
	v_mfma_f32_16x16x32_bf16 v[8:11], v[164:167], v[224:227], v[8:11]
	s_mul_hi_u32 s14, s15, s14
	s_add_i32 s15, s15, s14
	s_setprio 0
	s_setprio 1
	v_mfma_f32_16x16x32_bf16 v[60:63], v[168:171], v[184:187], v[60:63]
	s_mul_hi_u32 s14, s8, s15
	s_mul_i32 s15, s14, s12
	v_mfma_f32_16x16x32_bf16 v[52:55], v[176:179], v[184:187], v[52:55]
	s_sub_i32 s8, s8, s15
	s_add_i32 s36, s14, 1
	v_mfma_f32_16x16x32_bf16 v[44:47], v[168:171], v[192:195], v[44:47]
	s_sub_i32 s15, s8, s12
	s_cmp_ge_u32 s8, s12
	v_mfma_f32_16x16x32_bf16 v[36:39], v[176:179], v[192:195], v[36:39]
	s_cselect_b32 s14, s36, s14
	s_cselect_b32 s8, s15, s8
	v_mfma_f32_16x16x32_bf16 v[28:31], v[168:171], v[212:215], v[28:31]
	s_add_i32 s15, s14, 1
	s_cmp_ge_u32 s8, s12
	v_mfma_f32_16x16x32_bf16 v[20:23], v[176:179], v[212:215], v[20:23]
	s_cselect_b32 s8, s15, s14
	s_xor_b32 s8, s8, s13
	v_mfma_f32_16x16x32_bf16 v[12:15], v[168:171], v[220:223], v[12:15]
	s_sub_i32 s8, s8, s13
	s_mul_i32 s11, s8, s11
	v_mfma_f32_16x16x32_bf16 v[4:7], v[176:179], v[220:223], v[4:7]
	s_sub_i32 s9, s9, s11
	s_add_i32 s10, s10, s9
	v_mfma_f32_16x16x32_bf16 v[60:63], v[172:175], v[188:191], v[60:63]
	s_ashr_i32 s11, s10, 31
	s_lshl_b64 s[12:13], s[10:11], 19
	v_mfma_f32_16x16x32_bf16 v[52:55], v[180:183], v[188:191], v[52:55]
	s_add_u32 s12, s38, s12
	s_addc_u32 s13, s39, s13
	v_mfma_f32_16x16x32_bf16 v[44:47], v[172:175], v[196:199], v[44:47]
	s_and_b64 s[14:15], s[2:3], exec
	s_cselect_b32 s11, s13, s47
	v_mfma_f32_16x16x32_bf16 v[36:39], v[180:183], v[196:199], v[36:39]
	s_cselect_b32 s59, s12, s46
	s_ashr_i32 s9, s8, 31
	v_mfma_f32_16x16x32_bf16 v[28:31], v[172:175], v[216:219], v[28:31]
	s_lshl_b64 s[14:15], s[8:9], 19
	s_add_u32 s14, s40, s14
	v_mfma_f32_16x16x32_bf16 v[20:23], v[180:183], v[216:219], v[20:23]
	s_addc_u32 s15, s41, s15
	s_and_b64 s[36:37], s[2:3], exec
	v_mfma_f32_16x16x32_bf16 v[12:15], v[172:175], v[224:227], v[12:15]
	s_cselect_b32 s9, s15, s53
	s_cselect_b32 s60, s14, s52
	v_mfma_f32_16x16x32_bf16 v[4:7], v[180:183], v[224:227], v[4:7]
	s_setprio 0
	s_barrier
	s_add_i32 s62, s62, 2
	s_add_u32 s46, s46, 0x100
	s_addc_u32 s47, s47, 0
	s_add_u32 s52, s52, 0x100
	s_addc_u32 s53, s53, 0
	s_cmp_gt_u32 s62, 13
	s_cbranch_scc1 .Lpeel_done_727
